# speedup vs baseline: 1.0016x; 1.0016x over previous
.LBB2_9:
	s_waitcnt lgkmcnt(12)
	v_mfma_f32_32x32x16_f16 v[16:31], v[140:143], v[172:175], v[16:31]
	v_exp_f32_e32 v99, v99
	v_exp_f32_e32 v100, v100
	v_exp_f32_e32 v101, v101
	v_add_u32_e32 v60, s29, v190
	ds_read_b128 v[56:59], v60
	ds_read_b128 v[176:179], v60 offset:512
	s_waitcnt lgkmcnt(12)
	v_mfma_f32_32x32x16_f16 v[0:15], v[136:139], v[64:67], v[0:15]
	v_exp_f32_e32 v102, v102
	v_exp_f32_e32 v103, v103
	v_exp_f32_e32 v104, v104
	ds_read_b128 v[172:175], v60 offset:2048
	ds_read_b128 v[168:171], v60 offset:2560
	s_waitcnt lgkmcnt(12)
	v_mfma_f32_32x32x16_f16 v[16:31], v[136:139], v[68:71], v[16:31]
	v_exp_f32_e32 v105, v105
	v_exp_f32_e32 v106, v106
	v_exp_f32_e32 v107, v107
	ds_read_b128 v[164:167], v60 offset:4096
	ds_read_b128 v[160:163], v60 offset:4608
	s_waitcnt lgkmcnt(12)
	v_mfma_f32_32x32x16_f16 v[0:15], v[132:135], v[76:79], v[0:15]
	v_exp_f32_e32 v108, v108
	v_exp_f32_e32 v109, v109
	v_exp_f32_e32 v110, v110
	ds_read_b128 v[156:159], v60 offset:6144
	ds_read_b128 v[152:155], v60 offset:6656
	s_waitcnt lgkmcnt(12)
	v_mfma_f32_32x32x16_f16 v[16:31], v[132:135], v[48:51], v[16:31]
	s_waitcnt vmcnt(2) lgkmcnt(0)
	s_barrier
	v_exp_f32_e32 v111, v111
	v_exp_f32_e32 v80, v80
	v_exp_f32_e32 v81, v81
	v_mfma_f32_32x32x16_f16 v[0:15], v[128:131], v[72:75], v[0:15]
	v_exp_f32_e32 v82, v82
	v_exp_f32_e32 v83, v83
	v_exp_f32_e32 v84, v84
	s_waitcnt lgkmcnt(8)
	v_mfma_f32_32x32x16_f16 v[16:31], v[128:131], v[52:55], v[16:31]
	v_exp_f32_e32 v85, v85
	v_exp_f32_e32 v86, v86
	v_exp_f32_e32 v87, v87
	s_andn2_b64 vcc, exec, s[8:9]
	s_cbranch_vccnz .LBB2_11
	v_add_u32_e32 v64, s23, v184
	ds_read_b128 v[48:51], v64 offset:49248
	ds_read_b128 v[52:55], v64 offset:49216
	ds_read_b128 v[60:63], v64 offset:49184
	ds_read_b128 v[64:67], v64 offset:49152
	s_waitcnt lgkmcnt(3)
	v_pk_mul_f32 v[12:13], v[12:13], v[48:49]
	s_waitcnt lgkmcnt(2)
	v_pk_mul_f32 v[8:9], v[8:9], v[52:53]
	s_waitcnt lgkmcnt(1)
	v_pk_mul_f32 v[4:5], v[4:5], v[60:61]
	v_pk_mul_f32 v[14:15], v[14:15], v[50:51]
	v_pk_mul_f32 v[10:11], v[10:11], v[54:55]
	v_pk_mul_f32 v[6:7], v[6:7], v[62:63]
	s_waitcnt lgkmcnt(0)
	v_pk_mul_f32 v[2:3], v[2:3], v[66:67]
	v_pk_mul_f32 v[0:1], v[0:1], v[64:65]
	v_pk_mul_f32 v[28:29], v[28:29], v[48:49]
	v_pk_mul_f32 v[24:25], v[24:25], v[52:53]
	v_pk_mul_f32 v[20:21], v[20:21], v[60:61]
	v_pk_mul_f32 v[30:31], v[30:31], v[50:51]
	v_pk_mul_f32 v[26:27], v[26:27], v[54:55]
	v_pk_mul_f32 v[22:23], v[22:23], v[62:63]
	v_pk_mul_f32 v[18:19], v[18:19], v[66:67]
	v_pk_mul_f32 v[16:17], v[16:17], v[64:65]

.LBB2_15:
	s_waitcnt lgkmcnt(12)
	v_mfma_f32_32x32x16_f16 v[16:31], v[140:143], v[144:147], v[16:31]
	v_exp_f32_e32 v67, v67
	v_exp_f32_e32 v68, v68
	v_exp_f32_e32 v69, v69
	v_add_u32_e32 v88, s33, v190
	ds_read_b128 v[172:175], v88
	ds_read_b128 v[168:171], v88 offset:512
	s_waitcnt lgkmcnt(12)
	v_mfma_f32_32x32x16_f16 v[0:15], v[136:139], v[96:99], v[0:15]
	v_exp_f32_e32 v70, v70
	v_exp_f32_e32 v71, v71
	v_exp_f32_e32 v72, v72
	ds_read_b128 v[164:167], v88 offset:2048
	ds_read_b128 v[160:163], v88 offset:2560
	s_waitcnt lgkmcnt(12)
	v_mfma_f32_32x32x16_f16 v[16:31], v[136:139], v[100:103], v[16:31]
	v_exp_f32_e32 v73, v73
	v_exp_f32_e32 v74, v74
	v_exp_f32_e32 v75, v75
	ds_read_b128 v[156:159], v88 offset:4096
	ds_read_b128 v[152:155], v88 offset:4608
	s_waitcnt lgkmcnt(12)
	v_mfma_f32_32x32x16_f16 v[0:15], v[132:135], v[104:107], v[0:15]
	v_exp_f32_e32 v76, v76
	v_exp_f32_e32 v77, v77
	v_exp_f32_e32 v78, v78
	ds_read_b128 v[148:151], v88 offset:6144
	ds_read_b128 v[144:147], v88 offset:6656
	s_waitcnt lgkmcnt(12)
	v_mfma_f32_32x32x16_f16 v[16:31], v[132:135], v[80:83], v[16:31]
	s_waitcnt vmcnt(2) lgkmcnt(0)
	s_barrier
	v_exp_f32_e32 v79, v79
	v_exp_f32_e32 v48, v48
	v_exp_f32_e32 v49, v49
	v_mfma_f32_32x32x16_f16 v[0:15], v[128:131], v[108:111], v[0:15]
	v_exp_f32_e32 v50, v50
	v_exp_f32_e32 v51, v51
	v_exp_f32_e32 v52, v52
	s_waitcnt lgkmcnt(8)
	v_mfma_f32_32x32x16_f16 v[16:31], v[128:131], v[84:87], v[16:31]
	v_exp_f32_e32 v53, v53
	v_exp_f32_e32 v54, v54
	v_exp_f32_e32 v55, v55
	s_andn2_b64 vcc, exec, s[8:9]
	s_cbranch_vccnz .LBB2_17
	v_add_u32_e32 v92, s23, v184
	ds_read_b128 v[80:83], v92 offset:49248
	ds_read_b128 v[84:87], v92 offset:49216
	ds_read_b128 v[88:91], v92 offset:49152
	ds_read_b128 v[92:95], v92 offset:49184
	s_waitcnt lgkmcnt(3)
	v_pk_mul_f32 v[14:15], v[14:15], v[82:83]
	v_pk_mul_f32 v[12:13], v[12:13], v[80:81]
	s_waitcnt lgkmcnt(2)
	v_pk_mul_f32 v[10:11], v[10:11], v[86:87]
	v_pk_mul_f32 v[8:9], v[8:9], v[84:85]
	s_waitcnt lgkmcnt(0)
	v_pk_mul_f32 v[6:7], v[6:7], v[94:95]
	v_pk_mul_f32 v[4:5], v[4:5], v[92:93]
	v_pk_mul_f32 v[2:3], v[2:3], v[90:91]
	v_pk_mul_f32 v[0:1], v[0:1], v[88:89]
	v_pk_mul_f32 v[30:31], v[30:31], v[82:83]
	v_pk_mul_f32 v[28:29], v[28:29], v[80:81]
	v_pk_mul_f32 v[26:27], v[26:27], v[86:87]
	v_pk_mul_f32 v[24:25], v[24:25], v[84:85]
	v_pk_mul_f32 v[22:23], v[22:23], v[94:95]
	v_pk_mul_f32 v[20:21], v[20:21], v[92:93]
	v_pk_mul_f32 v[18:19], v[18:19], v[90:91]
	v_pk_mul_f32 v[16:17], v[16:17], v[88:89]
